# stack12 + unit-header-top fragment ds_reads (7 GEMM phases) + per-segment s_setprio flips removed from the GEMM K-loops
# baseline (speedup 1.0000x reference)
.LBB0_159:
	s_setprio 0
	v_readlane_b32 s30, v254, 1
	v_readlane_b32 s31, v254, 2
	s_mov_b32 s15, s99
	s_add_i32 s63, s63, 1
	s_mul_i32 s12, s63, s54
	s_waitcnt lgkmcnt(0)
	ds_read_b128 v[90:93], v197
	ds_read_b128 v[94:97], v197 offset:1024
	ds_read_b128 v[98:101], v197 offset:2048
	ds_read_b128 v[102:105], v197 offset:3072
	ds_read_b128 v[146:149], v198
	ds_read_b128 v[150:153], v198 offset:1024
	ds_read_b128 v[180:183], v198 offset:2048
	ds_read_b128 v[184:187], v198 offset:3072
	ds_read_b128 v[188:191], v199
	ds_read_b128 v[192:195], v199 offset:1024
	ds_read_b128 v[200:203], v199 offset:2048
	ds_read_b128 v[204:207], v199 offset:3072
	ds_read_b128 v[208:211], v199 offset:4096
	ds_read_b128 v[216:219], v199 offset:5120
	ds_read_b128 v[220:223], v199 offset:6144
	ds_read_b128 v[224:227], v199 offset:7168
	s_mul_hi_u32 s13, s63, s15
	s_add_i32 s13, s13, s12
	s_mul_i32 s12, s63, s15
	v_readlane_b32 s15, v254, 14
	s_add_u32 s30, s12, s15
	s_addc_u32 s31, s13, s55
	v_cmp_gt_i64_e32 vcc, s[30:31], v[178:179]
	v_cmp_lt_i64_e64 s[12:13], s[30:31], v[176:177]
	s_cbranch_vccnz .LBB0_161
	s_ashr_i32 s15, s30, 31
	s_lshr_b32 s15, s15, 29
	s_add_i32 s15, s30, s15
	s_ashr_i32 s26, s15, 3
	s_and_b32 s15, s15, -8
	s_sub_i32 s15, s30, s15
	s_cmp_lt_i32 s15, 0
	s_cselect_b32 s27, s56, 0x140
	s_mul_i32 s15, s15, s27
	s_add_i32 s15, s15, s26
	s_mul_hi_i32 s26, s15, 0x66666667
	s_lshr_b32 s27, s26, 31
	s_ashr_i32 s26, s26, 6
	s_add_i32 s26, s26, s27
	s_lshl_b32 s27, s26, 3
	s_sub_i32 s28, 0x80, s27
	s_min_i32 s28, s28, 8
	s_abs_i32 s29, s28
	v_cvt_f32_u32_e32 v2, s29
	s_sub_i32 s31, 0, s29
	s_mulk_i32 s26, 0xa0
	s_sub_i32 s15, s15, s26
	v_rcp_iflag_f32_e32 v2, v2
	s_abs_i32 s26, s15
	s_xor_b32 s30, s15, s28
	s_ashr_i32 s30, s30, 31
	v_mul_f32_e32 v2, 0x4f7ffffe, v2
	v_cvt_u32_f32_e32 v2, v2
	s_nop 0
	v_readfirstlane_b32 s34, v2
	s_mul_i32 s31, s31, s34
	s_mul_hi_u32 s31, s34, s31
	s_add_i32 s34, s34, s31
	s_mul_hi_u32 s31, s26, s34
	s_mul_i32 s34, s31, s29
	s_sub_i32 s26, s26, s34
	s_add_i32 s35, s31, 1
	s_sub_i32 s34, s26, s29
	s_cmp_ge_u32 s26, s29
	s_cselect_b32 s31, s35, s31
	s_cselect_b32 s26, s34, s26
	s_add_i32 s34, s31, 1
	s_cmp_ge_u32 s26, s29
	s_cselect_b32 s26, s34, s31
	s_xor_b32 s26, s26, s30
	s_sub_i32 s26, s26, s30
	s_mul_i32 s28, s26, s28
	s_sub_i32 s15, s15, s28
	s_add_i32 s28, s27, s15
.LBB0_161:
	s_ashr_i32 s29, s28, 31
	s_lshl_b64 s[30:31], s[28:29], 20
	v_readlane_b32 s34, v254, 18
	v_readlane_b32 s35, v254, 19
	s_add_u32 s30, s34, s30
	s_addc_u32 s31, s35, s31
	s_and_b64 s[34:35], s[12:13], exec
	s_cselect_b32 s15, s31, s17
	s_cselect_b32 s29, s30, s16
	s_ashr_i32 s27, s26, 31
	s_lshl_b64 s[34:35], s[26:27], 20
	s_add_u32 s34, s33, s34
	s_addc_u32 s35, s42, s35
	s_and_b64 s[38:39], s[12:13], exec
	s_cselect_b32 s27, s35, s37
	s_cselect_b32 s40, s34, s36
	s_add_u32 s16, s16, 0x80080
	s_addc_u32 s17, s17, 0
	s_add_u32 s41, s36, 0x100
	s_addc_u32 s64, s37, 0
	s_mov_b32 s65, -2
	s_add_u32 s36, s16, 0xfff80080
	s_addc_u32 s37, s17, -1
	s_cmp_eq_u32 s65, 28
	s_cselect_b32 s39, s15, s37
	s_cselect_b32 s38, s29, s36
	s_cselect_b32 s37, s27, s64
	s_cselect_b32 s36, s40, s41
	v_lshl_add_u64 v[212:213], s[16:17], 0, v[172:173]
	s_add_i32 m0, s44, 0xc000
	global_load_lds_dwordx4 v[212:213], off
	v_lshl_add_u64 v[212:213], s[16:17], 0, v[174:175]
	s_add_i32 m0, s44, 0xe000
	s_nop 0
	global_load_lds_dwordx4 v[212:213], off
	s_waitcnt vmcnt(8)
	s_waitcnt lgkmcnt(0)
	s_barrier
	v_mfma_f32_16x16x32_bf16 v[70:73], v[90:93], v[188:191], 0
	v_mfma_f32_16x16x32_bf16 v[66:69], v[98:101], v[188:191], 0
	v_mfma_f32_16x16x32_bf16 v[54:57], v[90:93], v[200:203], 0
	v_mfma_f32_16x16x32_bf16 v[50:53], v[98:101], v[200:203], 0
	v_mfma_f32_16x16x32_bf16 v[46:49], v[90:93], v[208:211], 0
	v_mfma_f32_16x16x32_bf16 v[42:45], v[98:101], v[208:211], 0
	v_mfma_f32_16x16x32_bf16 v[38:41], v[90:93], v[220:223], 0
	v_mfma_f32_16x16x32_bf16 v[34:37], v[98:101], v[220:223], 0
	v_mfma_f32_16x16x32_bf16 v[70:73], v[94:97], v[192:195], v[70:73]
	v_mfma_f32_16x16x32_bf16 v[66:69], v[102:105], v[192:195], v[66:69]
	v_mfma_f32_16x16x32_bf16 v[54:57], v[94:97], v[204:207], v[54:57]
	v_mfma_f32_16x16x32_bf16 v[50:53], v[102:105], v[204:207], v[50:53]
	v_mfma_f32_16x16x32_bf16 v[46:49], v[94:97], v[216:219], v[46:49]
	v_mfma_f32_16x16x32_bf16 v[42:45], v[102:105], v[216:219], v[42:45]
	v_mfma_f32_16x16x32_bf16 v[38:41], v[94:97], v[224:227], v[38:41]
	v_mfma_f32_16x16x32_bf16 v[34:37], v[102:105], v[224:227], v[34:37]
	v_mfma_f32_16x16x32_bf16 v[142:145], v[146:149], v[188:191], 0
	v_mfma_f32_16x16x32_bf16 v[138:141], v[180:183], v[188:191], 0
	v_mfma_f32_16x16x32_bf16 v[134:137], v[146:149], v[200:203], 0
	v_mfma_f32_16x16x32_bf16 v[130:133], v[180:183], v[200:203], 0
	v_mfma_f32_16x16x32_bf16 v[126:129], v[146:149], v[208:211], 0
	v_mfma_f32_16x16x32_bf16 v[122:125], v[180:183], v[208:211], 0
	v_mfma_f32_16x16x32_bf16 v[118:121], v[146:149], v[220:223], 0
	v_mfma_f32_16x16x32_bf16 v[114:117], v[180:183], v[220:223], 0
	v_mfma_f32_16x16x32_bf16 v[142:145], v[150:153], v[192:195], v[142:145]
	v_mfma_f32_16x16x32_bf16 v[138:141], v[184:187], v[192:195], v[138:141]
	v_mfma_f32_16x16x32_bf16 v[134:137], v[150:153], v[204:207], v[134:137]
	v_mfma_f32_16x16x32_bf16 v[130:133], v[184:187], v[204:207], v[130:133]
	v_mfma_f32_16x16x32_bf16 v[126:129], v[150:153], v[216:219], v[126:129]
	v_mfma_f32_16x16x32_bf16 v[122:125], v[184:187], v[216:219], v[122:125]
	v_mfma_f32_16x16x32_bf16 v[118:121], v[150:153], v[224:227], v[118:121]
	v_mfma_f32_16x16x32_bf16 v[114:117], v[184:187], v[224:227], v[114:117]
	s_barrier
	s_add_i32 s66, s57, s43
	v_lshl_add_u64 v[212:213], s[36:37], 0, v[156:157]
	s_mov_b32 m0, s66
	ds_read_b128 v[188:191], v199 offset:16384
	ds_read_b128 v[192:195], v199 offset:17408
	ds_read_b128 v[200:203], v199 offset:18432
	ds_read_b128 v[204:207], v199 offset:19456
	ds_read_b128 v[208:211], v199 offset:20480
	ds_read_b128 v[216:219], v199 offset:21504
	ds_read_b128 v[220:223], v199 offset:22528
	ds_read_b128 v[224:227], v199 offset:23552
	global_load_lds_dwordx4 v[212:213], off
	s_add_i32 m0, s66, 0x2000
	s_add_u32 s66, s36, 0x80000
	v_lshl_add_u64 v[214:215], s[36:37], 0, v[160:161]
	s_addc_u32 s67, s37, 0
	s_add_i32 s68, s58, s43
	global_load_lds_dwordx4 v[214:215], off
	v_lshl_add_u64 v[228:229], s[66:67], 0, v[156:157]
	s_mov_b32 m0, s68
	v_lshl_add_u64 v[230:231], s[38:39], 0, v[158:159]
	global_load_lds_dwordx4 v[228:229], off
	v_lshl_add_u64 v[228:229], s[66:67], 0, v[160:161]
	s_add_i32 m0, s68, 0x2000
	s_nop 0
	global_load_lds_dwordx4 v[228:229], off
	v_lshl_add_u64 v[228:229], s[38:39], 0, v[154:155]
	s_mov_b32 m0, s44
	s_nop 0
	global_load_lds_dwordx4 v[228:229], off
	s_mov_b32 m0, s45
	s_nop 0
	global_load_lds_dwordx4 v[230:231], off
	s_waitcnt vmcnt(8)
	s_waitcnt lgkmcnt(0)
	s_barrier
	v_mfma_f32_16x16x32_bf16 v[30:33], v[90:93], v[188:191], 0
	v_mfma_f32_16x16x32_bf16 v[26:29], v[98:101], v[188:191], 0
	v_mfma_f32_16x16x32_bf16 v[22:25], v[90:93], v[200:203], 0
	v_mfma_f32_16x16x32_bf16 v[18:21], v[98:101], v[200:203], 0
	v_mfma_f32_16x16x32_bf16 v[14:17], v[90:93], v[208:211], 0
	v_mfma_f32_16x16x32_bf16 v[10:13], v[98:101], v[208:211], 0
	v_mfma_f32_16x16x32_bf16 v[6:9], v[90:93], v[220:223], 0
	v_mfma_f32_16x16x32_bf16 v[2:5], v[98:101], v[220:223], 0
	v_mfma_f32_16x16x32_bf16 v[30:33], v[94:97], v[192:195], v[30:33]
	v_mfma_f32_16x16x32_bf16 v[26:29], v[102:105], v[192:195], v[26:29]
	v_mfma_f32_16x16x32_bf16 v[22:25], v[94:97], v[204:207], v[22:25]
	v_mfma_f32_16x16x32_bf16 v[18:21], v[102:105], v[204:207], v[18:21]
	v_mfma_f32_16x16x32_bf16 v[14:17], v[94:97], v[216:219], v[14:17]
	v_mfma_f32_16x16x32_bf16 v[10:13], v[102:105], v[216:219], v[10:13]
	v_mfma_f32_16x16x32_bf16 v[6:9], v[94:97], v[224:227], v[6:9]
	v_mfma_f32_16x16x32_bf16 v[2:5], v[102:105], v[224:227], v[2:5]
	v_mfma_f32_16x16x32_bf16 v[86:89], v[146:149], v[200:203], 0
	v_mfma_f32_16x16x32_bf16 v[82:85], v[180:183], v[200:203], 0
	v_mfma_f32_16x16x32_bf16 v[78:81], v[146:149], v[208:211], 0
	v_mfma_f32_16x16x32_bf16 v[74:77], v[180:183], v[208:211], 0
	v_mfma_f32_16x16x32_bf16 v[62:65], v[146:149], v[220:223], 0
	v_mfma_f32_16x16x32_bf16 v[58:61], v[180:183], v[220:223], 0
	v_mfma_f32_16x16x32_bf16 v[90:93], v[146:149], v[188:191], 0
	v_mfma_f32_16x16x32_bf16 v[94:97], v[180:183], v[188:191], 0
	v_mfma_f32_16x16x32_bf16 v[86:89], v[150:153], v[204:207], v[86:89]
	v_mfma_f32_16x16x32_bf16 v[82:85], v[184:187], v[204:207], v[82:85]
	v_mfma_f32_16x16x32_bf16 v[78:81], v[150:153], v[216:219], v[78:81]
	v_mfma_f32_16x16x32_bf16 v[74:77], v[184:187], v[216:219], v[74:77]
	v_mfma_f32_16x16x32_bf16 v[62:65], v[150:153], v[224:227], v[62:65]
	v_mfma_f32_16x16x32_bf16 v[58:61], v[184:187], v[224:227], v[58:61]
	v_mfma_f32_16x16x32_bf16 v[90:93], v[150:153], v[192:195], v[90:93]
	v_mfma_f32_16x16x32_bf16 v[94:97], v[184:187], v[192:195], v[94:97]
	s_barrier
	s_add_i32 s66, 0, 0x18000
	s_add_i32 s67, 0, 0x1c000
	v_add_u32_e32 v110, s66, v165
	v_add_u32_e32 v162, s67, v165
	ds_read_b128 v[98:101], v110
	ds_read_b128 v[102:105], v110 offset:1024
	ds_read_b128 v[106:109], v110 offset:2048
	ds_read_b128 v[110:113], v110 offset:3072
	ds_read_b128 v[146:149], v162
	ds_read_b128 v[150:153], v162 offset:1024
	ds_read_b128 v[180:183], v162 offset:2048
	ds_read_b128 v[184:187], v162 offset:3072
	s_add_u32 s38, s38, 0x80000
	s_addc_u32 s39, s39, 0
	s_mov_b32 m0, s47
	v_lshl_add_u64 v[232:233], s[38:39], 0, v[154:155]
	ds_read_b128 v[188:191], v199 offset:32768
	ds_read_b128 v[192:195], v199 offset:33792
	ds_read_b128 v[200:203], v199 offset:34816
	ds_read_b128 v[204:207], v199 offset:35840
	ds_read_b128 v[208:211], v199 offset:36864
	ds_read_b128 v[216:219], v199 offset:37888
	ds_read_b128 v[220:223], v199 offset:38912
	ds_read_b128 v[224:227], v199 offset:39936
	global_load_lds_dwordx4 v[232:233], off
	v_lshl_add_u64 v[232:233], s[38:39], 0, v[158:159]
	s_mov_b32 m0, s48
	s_nop 0
	global_load_lds_dwordx4 v[232:233], off
	s_waitcnt vmcnt(8)
	s_waitcnt lgkmcnt(0)
	s_barrier
	v_mfma_f32_16x16x32_bf16 v[70:73], v[98:101], v[188:191], v[70:73]
	v_mfma_f32_16x16x32_bf16 v[66:69], v[106:109], v[188:191], v[66:69]
	v_mfma_f32_16x16x32_bf16 v[54:57], v[98:101], v[200:203], v[54:57]
	v_mfma_f32_16x16x32_bf16 v[50:53], v[106:109], v[200:203], v[50:53]
	v_mfma_f32_16x16x32_bf16 v[46:49], v[98:101], v[208:211], v[46:49]
	v_mfma_f32_16x16x32_bf16 v[42:45], v[106:109], v[208:211], v[42:45]
	v_mfma_f32_16x16x32_bf16 v[38:41], v[98:101], v[220:223], v[38:41]
	v_mfma_f32_16x16x32_bf16 v[34:37], v[106:109], v[220:223], v[34:37]
	v_mfma_f32_16x16x32_bf16 v[70:73], v[102:105], v[192:195], v[70:73]
	v_mfma_f32_16x16x32_bf16 v[66:69], v[110:113], v[192:195], v[66:69]
	v_mfma_f32_16x16x32_bf16 v[54:57], v[102:105], v[204:207], v[54:57]
	v_mfma_f32_16x16x32_bf16 v[50:53], v[110:113], v[204:207], v[50:53]
	v_mfma_f32_16x16x32_bf16 v[46:49], v[102:105], v[216:219], v[46:49]
	v_mfma_f32_16x16x32_bf16 v[42:45], v[110:113], v[216:219], v[42:45]
	v_mfma_f32_16x16x32_bf16 v[38:41], v[102:105], v[224:227], v[38:41]
	v_mfma_f32_16x16x32_bf16 v[34:37], v[110:113], v[224:227], v[34:37]
	v_mfma_f32_16x16x32_bf16 v[142:145], v[146:149], v[188:191], v[142:145]
	v_mfma_f32_16x16x32_bf16 v[138:141], v[180:183], v[188:191], v[138:141]
	v_mfma_f32_16x16x32_bf16 v[134:137], v[146:149], v[200:203], v[134:137]
	v_mfma_f32_16x16x32_bf16 v[130:133], v[180:183], v[200:203], v[130:133]
	v_mfma_f32_16x16x32_bf16 v[126:129], v[146:149], v[208:211], v[126:129]
	v_mfma_f32_16x16x32_bf16 v[122:125], v[180:183], v[208:211], v[122:125]
	v_mfma_f32_16x16x32_bf16 v[118:121], v[146:149], v[220:223], v[118:121]
	v_mfma_f32_16x16x32_bf16 v[114:117], v[180:183], v[220:223], v[114:117]
	v_mfma_f32_16x16x32_bf16 v[142:145], v[150:153], v[192:195], v[142:145]
	v_mfma_f32_16x16x32_bf16 v[138:141], v[184:187], v[192:195], v[138:141]
	v_mfma_f32_16x16x32_bf16 v[134:137], v[150:153], v[204:207], v[134:137]
	v_mfma_f32_16x16x32_bf16 v[130:133], v[184:187], v[204:207], v[130:133]
	v_mfma_f32_16x16x32_bf16 v[126:129], v[150:153], v[216:219], v[126:129]
	v_mfma_f32_16x16x32_bf16 v[122:125], v[184:187], v[216:219], v[122:125]
	v_mfma_f32_16x16x32_bf16 v[118:121], v[150:153], v[224:227], v[118:121]
	v_mfma_f32_16x16x32_bf16 v[114:117], v[184:187], v[224:227], v[114:117]
	s_barrier
	s_add_i32 s38, s66, s43
	v_lshl_add_u64 v[212:213], v[212:213], 0, s[18:19]
	s_mov_b32 m0, s38
	ds_read_b128 v[188:191], v199 offset:49152
	ds_read_b128 v[192:195], v199 offset:50176
	ds_read_b128 v[200:203], v199 offset:51200
	ds_read_b128 v[204:207], v199 offset:52224
	ds_read_b128 v[208:211], v199 offset:53248
	ds_read_b128 v[216:219], v199 offset:54272
	ds_read_b128 v[220:223], v199 offset:55296
	ds_read_b128 v[224:227], v199 offset:56320
	global_load_lds_dwordx4 v[212:213], off
	s_add_i32 m0, s38, 0x2000
	s_add_u32 s36, s36, 0x80080
	v_lshl_add_u64 v[212:213], v[214:215], 0, s[18:19]
	s_addc_u32 s37, s37, 0
	s_add_i32 s38, s67, s43
	global_load_lds_dwordx4 v[212:213], off
	v_lshl_add_u64 v[212:213], s[36:37], 0, v[156:157]
	s_mov_b32 m0, s38
	s_nop 0
	global_load_lds_dwordx4 v[212:213], off
	v_lshl_add_u64 v[212:213], s[36:37], 0, v[160:161]
	s_add_i32 m0, s38, 0x2000
	s_nop 0
	global_load_lds_dwordx4 v[212:213], off
	v_lshl_add_u64 v[212:213], v[228:229], 0, s[18:19]
	s_mov_b32 m0, s52
	s_nop 0
	global_load_lds_dwordx4 v[212:213], off
	v_lshl_add_u64 v[212:213], v[230:231], 0, s[18:19]
	s_mov_b32 m0, s53
	s_nop 0
	global_load_lds_dwordx4 v[212:213], off
	s_waitcnt vmcnt(8)
	s_waitcnt lgkmcnt(0)
	s_barrier
	v_mfma_f32_16x16x32_bf16 v[30:33], v[98:101], v[188:191], v[30:33]
	v_mfma_f32_16x16x32_bf16 v[26:29], v[106:109], v[188:191], v[26:29]
	v_mfma_f32_16x16x32_bf16 v[22:25], v[98:101], v[200:203], v[22:25]
	v_mfma_f32_16x16x32_bf16 v[18:21], v[106:109], v[200:203], v[18:21]
	v_mfma_f32_16x16x32_bf16 v[14:17], v[98:101], v[208:211], v[14:17]
	v_mfma_f32_16x16x32_bf16 v[10:13], v[106:109], v[208:211], v[10:13]
	v_mfma_f32_16x16x32_bf16 v[6:9], v[98:101], v[220:223], v[6:9]
	v_mfma_f32_16x16x32_bf16 v[2:5], v[106:109], v[220:223], v[2:5]
	v_mfma_f32_16x16x32_bf16 v[30:33], v[102:105], v[192:195], v[30:33]
	v_mfma_f32_16x16x32_bf16 v[26:29], v[110:113], v[192:195], v[26:29]
	v_mfma_f32_16x16x32_bf16 v[22:25], v[102:105], v[204:207], v[22:25]
	v_mfma_f32_16x16x32_bf16 v[18:21], v[110:113], v[204:207], v[18:21]
	v_mfma_f32_16x16x32_bf16 v[14:17], v[102:105], v[216:219], v[14:17]
	v_mfma_f32_16x16x32_bf16 v[10:13], v[110:113], v[216:219], v[10:13]
	v_mfma_f32_16x16x32_bf16 v[6:9], v[102:105], v[224:227], v[6:9]
	v_mfma_f32_16x16x32_bf16 v[2:5], v[110:113], v[224:227], v[2:5]
	v_mfma_f32_16x16x32_bf16 v[90:93], v[146:149], v[188:191], v[90:93]
	v_mfma_f32_16x16x32_bf16 v[110:113], v[150:153], v[192:195], v[90:93]
	v_mfma_f32_16x16x32_bf16 v[90:93], v[180:183], v[188:191], v[94:97]
	v_mfma_f32_16x16x32_bf16 v[86:89], v[146:149], v[200:203], v[86:89]
	v_mfma_f32_16x16x32_bf16 v[82:85], v[180:183], v[200:203], v[82:85]
	v_mfma_f32_16x16x32_bf16 v[78:81], v[146:149], v[208:211], v[78:81]
	v_mfma_f32_16x16x32_bf16 v[74:77], v[180:183], v[208:211], v[74:77]
	v_mfma_f32_16x16x32_bf16 v[62:65], v[146:149], v[220:223], v[62:65]
	v_mfma_f32_16x16x32_bf16 v[58:61], v[180:183], v[220:223], v[58:61]
	v_mfma_f32_16x16x32_bf16 v[106:109], v[184:187], v[192:195], v[90:93]
	v_mfma_f32_16x16x32_bf16 v[86:89], v[150:153], v[204:207], v[86:89]
	v_mfma_f32_16x16x32_bf16 v[82:85], v[184:187], v[204:207], v[82:85]
	v_mfma_f32_16x16x32_bf16 v[78:81], v[150:153], v[216:219], v[78:81]
	v_mfma_f32_16x16x32_bf16 v[74:77], v[184:187], v[216:219], v[74:77]
	v_mfma_f32_16x16x32_bf16 v[62:65], v[150:153], v[224:227], v[62:65]
	v_mfma_f32_16x16x32_bf16 v[58:61], v[184:187], v[224:227], v[58:61]
	s_barrier
	s_add_i32 s65, s65, 2
	s_add_u32 s16, s16, 0x100
	s_addc_u32 s17, s17, 0
	s_add_u32 s41, s41, 0x100
	s_addc_u32 s64, s64, 0
	s_cmp_gt_u32 s65, 29

.LBB0_1339:
	s_setprio 0
	v_readlane_b32 s24, v254, 1
	v_readlane_b32 s25, v254, 2
	s_mov_b32 s21, s99
	s_add_i32 s44, s44, 1
	s_mul_i32 s8, s44, s47
	s_waitcnt lgkmcnt(0)
	ds_read_b128 v[154:157], v150
	ds_read_b128 v[158:161], v150 offset:1024
	ds_read_b128 v[162:165], v150 offset:2048
	ds_read_b128 v[166:169], v150 offset:3072
	ds_read_b128 v[170:173], v151
	ds_read_b128 v[174:177], v151 offset:1024
	ds_read_b128 v[178:181], v151 offset:2048
	ds_read_b128 v[182:185], v151 offset:3072
	ds_read_b128 v[186:189], v152
	ds_read_b128 v[190:193], v152 offset:1024
	ds_read_b128 v[194:197], v152 offset:2048
	ds_read_b128 v[198:201], v152 offset:3072
	ds_read_b128 v[202:205], v152 offset:4096
	ds_read_b128 v[206:209], v152 offset:5120
	ds_read_b128 v[210:213], v152 offset:6144
	ds_read_b128 v[214:217], v152 offset:7168
	s_mul_hi_u32 s9, s44, s21
	s_add_i32 s9, s9, s8
	s_mul_i32 s8, s44, s21
	v_readlane_b32 s21, v254, 14
	s_add_u32 s24, s8, s21
	s_addc_u32 s25, s9, s33
	v_cmp_gt_i64_e32 vcc, s[24:25], v[144:145]
	v_cmp_lt_i64_e64 s[8:9], s[24:25], v[142:143]
	s_cbranch_vccnz .LBB0_1345
	s_ashr_i32 s20, s24, 31
	s_lshr_b32 s20, s20, 29
	s_add_i32 s22, s24, s20
	s_and_b32 s20, s22, -8
	s_sub_i32 s23, s24, s20
	s_cmp_gt_i32 s23, -1
	s_mov_b64 s[20:21], -1
	s_cbranch_scc0 .LBB0_1342
	s_lshl_b32 s24, s23, 7
	s_mov_b64 s[20:21], 0

.LBB0_1476:
	s_setprio 0
	v_readlane_b32 s22, v254, 1
	v_readlane_b32 s23, v254, 2
	s_mov_b32 s17, s99
	s_add_i32 s43, s43, 1
	s_mul_i32 s8, s43, s46
	s_waitcnt lgkmcnt(0)
	ds_read_b128 v[154:157], v150
	ds_read_b128 v[158:161], v150 offset:1024
	ds_read_b128 v[162:165], v150 offset:2048
	ds_read_b128 v[166:169], v150 offset:3072
	ds_read_b128 v[170:173], v151
	ds_read_b128 v[174:177], v151 offset:1024
	ds_read_b128 v[178:181], v151 offset:2048
	ds_read_b128 v[182:185], v151 offset:3072
	ds_read_b128 v[186:189], v152
	ds_read_b128 v[190:193], v152 offset:1024
	ds_read_b128 v[194:197], v152 offset:2048
	ds_read_b128 v[198:201], v152 offset:3072
	ds_read_b128 v[202:205], v152 offset:4096
	ds_read_b128 v[206:209], v152 offset:5120
	ds_read_b128 v[210:213], v152 offset:6144
	ds_read_b128 v[214:217], v152 offset:7168
	s_mul_hi_u32 s9, s43, s17
	s_add_i32 s9, s9, s8
	s_mul_i32 s8, s43, s17
	v_readlane_b32 s17, v254, 14
	s_add_u32 s22, s8, s17
	s_addc_u32 s23, s9, s37
	v_cmp_gt_i64_e32 vcc, s[22:23], v[146:147]
	v_cmp_lt_i64_e64 s[8:9], s[22:23], v[144:145]
	s_cbranch_vccnz .LBB0_1478
	s_ashr_i32 s16, s22, 31
	s_lshr_b32 s16, s16, 29
	s_add_i32 s16, s22, s16
	s_ashr_i32 s17, s16, 3
	s_and_b32 s16, s16, -8
	s_sub_i32 s16, s22, s16
	s_cmp_lt_i32 s16, 0
	s_cselect_b32 s18, s38, 0x2c0
	s_mul_i32 s16, s16, s18
	s_add_i32 s16, s16, s17
	s_mul_hi_i32 s17, s16, 0x2e8ba2e9
	s_lshr_b32 s18, s17, 31
	s_ashr_i32 s17, s17, 6
	s_add_i32 s17, s17, s18
	s_lshl_b32 s18, s17, 3
	s_sub_i32 s19, 0x80, s18
	s_min_i32 s19, s19, 8
	s_abs_i32 s22, s19
	v_cvt_f32_u32_e32 v2, s22
	s_sub_i32 s24, 0, s22
	s_mulk_i32 s17, 0x160
	s_sub_i32 s17, s16, s17
	v_rcp_iflag_f32_e32 v2, v2
	s_abs_i32 s16, s17
	s_xor_b32 s23, s17, s19
	s_ashr_i32 s23, s23, 31
	v_mul_f32_e32 v2, 0x4f7ffffe, v2
	v_cvt_u32_f32_e32 v2, v2
	s_nop 0
	v_readfirstlane_b32 s25, v2
	s_mul_i32 s24, s24, s25
	s_mul_hi_u32 s24, s25, s24
	s_add_i32 s25, s25, s24
	s_mul_hi_u32 s24, s16, s25
	s_mul_i32 s25, s24, s22
	s_sub_i32 s16, s16, s25
	s_add_i32 s27, s24, 1
	s_sub_i32 s25, s16, s22
	s_cmp_ge_u32 s16, s22
	s_cselect_b32 s24, s27, s24
	s_cselect_b32 s16, s25, s16
	s_add_i32 s25, s24, 1
	s_cmp_ge_u32 s16, s22
	s_cselect_b32 s16, s25, s24
	s_xor_b32 s16, s16, s23
	s_sub_i32 s16, s16, s23
	s_mul_i32 s19, s16, s19
	s_sub_i32 s17, s17, s19
	s_add_i32 s18, s18, s17

.LBB0_1551:
	s_setprio 0
	v_readlane_b32 s8, v254, 1
	v_readlane_b32 s9, v254, 2
	s_mov_b32 s8, s99
	s_add_i32 s43, s43, 1
	s_mul_i32 s0, s43, s46
	s_waitcnt lgkmcnt(0)
	ds_read_b128 v[154:157], v150
	ds_read_b128 v[158:161], v150 offset:1024
	ds_read_b128 v[162:165], v150 offset:2048
	ds_read_b128 v[166:169], v150 offset:3072
	ds_read_b128 v[170:173], v151
	ds_read_b128 v[174:177], v151 offset:1024
	ds_read_b128 v[178:181], v151 offset:2048
	ds_read_b128 v[182:185], v151 offset:3072
	ds_read_b128 v[186:189], v152
	ds_read_b128 v[190:193], v152 offset:1024
	ds_read_b128 v[194:197], v152 offset:2048
	ds_read_b128 v[198:201], v152 offset:3072
	ds_read_b128 v[202:205], v152 offset:4096
	ds_read_b128 v[206:209], v152 offset:5120
	ds_read_b128 v[210:213], v152 offset:6144
	ds_read_b128 v[214:217], v152 offset:7168
	s_mul_hi_u32 s1, s43, s8
	s_add_i32 s1, s1, s0
	s_mul_i32 s0, s43, s8
	v_readlane_b32 s8, v254, 14
	s_add_u32 s8, s0, s8
	s_addc_u32 s9, s1, s33
	v_cmp_gt_i64_e32 vcc, s[8:9], v[144:145]
	v_cmp_lt_i64_e64 s[0:1], s[8:9], v[142:143]
	s_cbranch_vccnz .LBB0_1557
	s_ashr_i32 s9, s8, 31
	s_lshr_b32 s9, s9, 29
	s_add_i32 s24, s8, s9
	s_and_b32 s9, s24, -8
	s_sub_i32 s25, s8, s9
	s_cmp_gt_i32 s25, -1
	s_mov_b64 s[8:9], -1
	s_cbranch_scc0 .LBB0_1554
	s_lshl_b32 s30, s25, 7
	s_mov_b64 s[8:9], 0

.LBB0_1694:
	s_setprio 0
	v_readlane_b32 s38, v254, 1
	v_readlane_b32 s39, v254, 2
	s_mov_b32 s35, s99
	s_add_i32 s57, s57, 1
	s_mul_i32 s10, s57, s63
	s_waitcnt lgkmcnt(0)
	ds_read_b128 v[156:159], v176
	ds_read_b128 v[160:163], v176 offset:1024
	ds_read_b128 v[164:167], v176 offset:2048
	ds_read_b128 v[168:171], v176 offset:3072
	ds_read_b128 v[180:183], v177
	ds_read_b128 v[184:187], v177 offset:1024
	ds_read_b128 v[188:191], v177 offset:2048
	ds_read_b128 v[192:195], v177 offset:3072
	ds_read_b128 v[196:199], v178
	ds_read_b128 v[200:203], v178 offset:1024
	ds_read_b128 v[204:207], v178 offset:2048
	ds_read_b128 v[208:211], v178 offset:3072
	ds_read_b128 v[212:215], v178 offset:4096
	ds_read_b128 v[216:219], v178 offset:5120
	ds_read_b128 v[220:223], v178 offset:6144
	ds_read_b128 v[224:227], v178 offset:7168
	s_mul_hi_u32 s11, s57, s35
	s_add_i32 s11, s11, s10
	s_mul_i32 s10, s57, s35
	v_readlane_b32 s35, v254, 14
	s_add_u32 s38, s10, s35
	s_addc_u32 s39, s11, s64
	v_cmp_gt_i64_e32 vcc, s[38:39], v[154:155]
	v_cmp_lt_i64_e64 s[10:11], s[38:39], v[152:153]
	s_cbranch_vccnz .LBB0_1696
	s_ashr_i32 s34, s38, 31
	s_lshr_b32 s34, s34, 29
	s_add_i32 s34, s38, s34
	s_ashr_i32 s35, s34, 3
	s_and_b32 s34, s34, -8
	s_sub_i32 s34, s38, s34
	s_cmp_lt_i32 s34, 0
	s_movk_i32 s36, 0x191
	s_cselect_b32 s36, s36, 0x190
	s_mul_i32 s34, s34, s36
	s_add_i32 s34, s34, s35
	s_mul_hi_i32 s35, s34, 0x51eb851f
	s_lshr_b32 s36, s35, 31
	s_ashr_i32 s35, s35, 6
	s_add_i32 s35, s35, s36
	s_lshl_b32 s36, s35, 3
	s_sub_i32 s37, 0x80, s36
	s_min_i32 s37, s37, 8
	s_abs_i32 s38, s37
	v_cvt_f32_u32_e32 v2, s38
	s_sub_i32 s40, 0, s38
	s_mulk_i32 s35, 0xc8
	s_sub_i32 s35, s34, s35
	v_rcp_iflag_f32_e32 v2, v2
	s_abs_i32 s34, s35
	s_xor_b32 s39, s35, s37
	s_ashr_i32 s39, s39, 31
	v_mul_f32_e32 v2, 0x4f7ffffe, v2
	v_cvt_u32_f32_e32 v2, v2
	s_nop 0
	v_readfirstlane_b32 s41, v2
	s_mul_i32 s40, s40, s41
	s_mul_hi_u32 s40, s41, s40
	s_add_i32 s41, s41, s40
	s_mul_hi_u32 s40, s34, s41
	s_mul_i32 s41, s40, s38
	s_sub_i32 s34, s34, s41
	s_add_i32 s43, s40, 1
	s_sub_i32 s41, s34, s38
	s_cmp_ge_u32 s34, s38
	s_cselect_b32 s40, s43, s40
	s_cselect_b32 s34, s41, s34
	s_add_i32 s41, s40, 1
	s_cmp_ge_u32 s34, s38
	s_cselect_b32 s34, s41, s40
	s_xor_b32 s34, s34, s39
	s_sub_i32 s34, s34, s39
	s_mul_i32 s37, s34, s37
	s_sub_i32 s35, s35, s37
	s_add_i32 s36, s36, s35
.LBB0_1696:
	s_ashr_i32 s37, s36, 31
	s_lshl_b64 s[38:39], s[36:37], 20
	s_add_u32 s38, s20, s38
	s_addc_u32 s39, s21, s39
	s_and_b64 s[40:41], s[10:11], exec
	s_cselect_b32 s37, s39, s47
	s_cselect_b32 s43, s38, s46
	s_ashr_i32 s35, s34, 31
	s_lshl_b64 s[40:41], s[34:35], 20
	s_add_u32 s40, s23, s40
	s_addc_u32 s41, s33, s41
	s_and_b64 s[50:51], s[10:11], exec
	s_cselect_b32 s35, s41, s49
	s_cselect_b32 s45, s40, s48
	s_lshl_b32 s50, s44, 8
	s_ashr_i32 s51, s50, 31
	v_lshl_add_u64 v[238:239], s[50:51], 2, v[140:141]
	global_load_dword v240, v[238:239], off
	global_load_dword v242, v[238:239], off offset:64
	global_load_dword v244, v[238:239], off offset:128
	global_load_dword v246, v[238:239], off offset:192
	global_load_dword v248, v[238:239], off offset:512
	global_load_dword v250, v[238:239], off offset:576
	global_load_dword v252, v[238:239], off offset:640
	global_load_dword v238, v[238:239], off offset:704
	s_add_u32 s46, s46, 0x80080
	s_addc_u32 s47, s47, 0
	s_add_u32 s69, s48, 0x100
	s_addc_u32 s70, s49, 0
	s_mov_b32 s71, -2
	s_waitcnt vmcnt(0)
	s_add_u32 s48, s46, 0xfff80080
	s_addc_u32 s49, s47, -1
	s_cmp_eq_u32 s71, 28
	s_cselect_b32 s51, s37, s49
	s_cselect_b32 s50, s43, s48
	s_cselect_b32 s49, s35, s70
	s_cselect_b32 s48, s45, s69
	v_lshl_add_u64 v[172:173], s[46:47], 0, v[148:149]
	s_add_i32 m0, s53, 0xc000
	global_load_lds_dwordx4 v[172:173], off
	v_lshl_add_u64 v[172:173], s[46:47], 0, v[150:151]
	s_add_i32 m0, s53, 0xe000
	s_nop 0
	global_load_lds_dwordx4 v[172:173], off
	s_waitcnt vmcnt(8)
	s_waitcnt lgkmcnt(0)
	s_barrier
	v_mfma_f32_16x16x32_bf16 v[126:129], v[156:159], v[196:199], 0
	v_mfma_f32_16x16x32_bf16 v[122:125], v[164:167], v[196:199], 0
	v_mfma_f32_16x16x32_bf16 v[118:121], v[156:159], v[204:207], 0
	v_mfma_f32_16x16x32_bf16 v[114:117], v[164:167], v[204:207], 0
	v_mfma_f32_16x16x32_bf16 v[110:113], v[156:159], v[212:215], 0
	v_mfma_f32_16x16x32_bf16 v[106:109], v[164:167], v[212:215], 0
	v_mfma_f32_16x16x32_bf16 v[102:105], v[156:159], v[220:223], 0
	v_mfma_f32_16x16x32_bf16 v[98:101], v[164:167], v[220:223], 0
	v_mfma_f32_16x16x32_bf16 v[126:129], v[160:163], v[200:203], v[126:129]
	v_mfma_f32_16x16x32_bf16 v[122:125], v[168:171], v[200:203], v[122:125]
	v_mfma_f32_16x16x32_bf16 v[118:121], v[160:163], v[208:211], v[118:121]
	v_mfma_f32_16x16x32_bf16 v[114:117], v[168:171], v[208:211], v[114:117]
	v_mfma_f32_16x16x32_bf16 v[110:113], v[160:163], v[216:219], v[110:113]
	v_mfma_f32_16x16x32_bf16 v[106:109], v[168:171], v[216:219], v[106:109]
	v_mfma_f32_16x16x32_bf16 v[102:105], v[160:163], v[224:227], v[102:105]
	v_mfma_f32_16x16x32_bf16 v[98:101], v[168:171], v[224:227], v[98:101]
	v_mfma_f32_16x16x32_bf16 v[38:41], v[180:183], v[196:199], 0
	v_mfma_f32_16x16x32_bf16 v[34:37], v[188:191], v[196:199], 0
	v_mfma_f32_16x16x32_bf16 v[46:49], v[180:183], v[204:207], 0
	v_mfma_f32_16x16x32_bf16 v[42:45], v[188:191], v[204:207], 0
	v_mfma_f32_16x16x32_bf16 v[54:57], v[180:183], v[212:215], 0
	v_mfma_f32_16x16x32_bf16 v[50:53], v[188:191], v[212:215], 0
	v_mfma_f32_16x16x32_bf16 v[62:65], v[180:183], v[220:223], 0
	v_mfma_f32_16x16x32_bf16 v[58:61], v[188:191], v[220:223], 0
	v_mfma_f32_16x16x32_bf16 v[38:41], v[184:187], v[200:203], v[38:41]
	v_mfma_f32_16x16x32_bf16 v[34:37], v[192:195], v[200:203], v[34:37]
	v_mfma_f32_16x16x32_bf16 v[46:49], v[184:187], v[208:211], v[46:49]
	v_mfma_f32_16x16x32_bf16 v[42:45], v[192:195], v[208:211], v[42:45]
	v_mfma_f32_16x16x32_bf16 v[54:57], v[184:187], v[216:219], v[54:57]
	v_mfma_f32_16x16x32_bf16 v[50:53], v[192:195], v[216:219], v[50:53]
	v_mfma_f32_16x16x32_bf16 v[62:65], v[184:187], v[224:227], v[62:65]
	v_mfma_f32_16x16x32_bf16 v[58:61], v[192:195], v[224:227], v[58:61]
	s_barrier
	s_add_i32 s72, s65, s52
	v_lshl_add_u64 v[172:173], s[48:49], 0, v[132:133]
	s_mov_b32 m0, s72
	ds_read_b128 v[196:199], v178 offset:16384
	ds_read_b128 v[200:203], v178 offset:17408
	ds_read_b128 v[204:207], v178 offset:18432
	ds_read_b128 v[208:211], v178 offset:19456
	ds_read_b128 v[212:215], v178 offset:20480
	ds_read_b128 v[216:219], v178 offset:21504
	ds_read_b128 v[220:223], v178 offset:22528
	ds_read_b128 v[224:227], v178 offset:23552
	global_load_lds_dwordx4 v[172:173], off
	s_add_i32 m0, s72, 0x2000
	s_add_u32 s72, s48, 0x80000
	v_lshl_add_u64 v[228:229], s[48:49], 0, v[136:137]
	s_addc_u32 s73, s49, 0
	s_add_i32 s74, s66, s52
	global_load_lds_dwordx4 v[228:229], off
	v_lshl_add_u64 v[230:231], s[72:73], 0, v[132:133]
	s_mov_b32 m0, s74
	v_lshl_add_u64 v[232:233], s[50:51], 0, v[134:135]
	global_load_lds_dwordx4 v[230:231], off
	v_lshl_add_u64 v[230:231], s[72:73], 0, v[136:137]
	s_add_i32 m0, s74, 0x2000
	s_nop 0
	global_load_lds_dwordx4 v[230:231], off
	v_lshl_add_u64 v[230:231], s[50:51], 0, v[130:131]
	s_mov_b32 m0, s53
	s_nop 0
	global_load_lds_dwordx4 v[230:231], off
	s_mov_b32 m0, s54
	s_nop 0
	global_load_lds_dwordx4 v[232:233], off
	s_waitcnt vmcnt(8)
	s_waitcnt lgkmcnt(0)
	s_barrier
	v_mfma_f32_16x16x32_bf16 v[94:97], v[156:159], v[196:199], 0
	v_mfma_f32_16x16x32_bf16 v[90:93], v[164:167], v[196:199], 0
	v_mfma_f32_16x16x32_bf16 v[86:89], v[156:159], v[204:207], 0
	v_mfma_f32_16x16x32_bf16 v[82:85], v[164:167], v[204:207], 0
	v_mfma_f32_16x16x32_bf16 v[78:81], v[156:159], v[212:215], 0
	v_mfma_f32_16x16x32_bf16 v[74:77], v[164:167], v[212:215], 0
	v_mfma_f32_16x16x32_bf16 v[70:73], v[156:159], v[220:223], 0
	v_mfma_f32_16x16x32_bf16 v[66:69], v[164:167], v[220:223], 0
	v_mfma_f32_16x16x32_bf16 v[94:97], v[160:163], v[200:203], v[94:97]
	v_mfma_f32_16x16x32_bf16 v[90:93], v[168:171], v[200:203], v[90:93]
	v_mfma_f32_16x16x32_bf16 v[86:89], v[160:163], v[208:211], v[86:89]
	v_mfma_f32_16x16x32_bf16 v[82:85], v[168:171], v[208:211], v[82:85]
	v_mfma_f32_16x16x32_bf16 v[78:81], v[160:163], v[216:219], v[78:81]
	v_mfma_f32_16x16x32_bf16 v[74:77], v[168:171], v[216:219], v[74:77]
	v_mfma_f32_16x16x32_bf16 v[70:73], v[160:163], v[224:227], v[70:73]
	v_mfma_f32_16x16x32_bf16 v[66:69], v[168:171], v[224:227], v[66:69]
	v_mfma_f32_16x16x32_bf16 v[6:9], v[180:183], v[196:199], 0
	v_mfma_f32_16x16x32_bf16 v[2:5], v[188:191], v[196:199], 0
	v_mfma_f32_16x16x32_bf16 v[18:21], v[180:183], v[204:207], 0
	v_mfma_f32_16x16x32_bf16 v[14:17], v[188:191], v[204:207], 0
	v_mfma_f32_16x16x32_bf16 v[26:29], v[180:183], v[212:215], 0
	v_mfma_f32_16x16x32_bf16 v[22:25], v[188:191], v[212:215], 0
	v_mfma_f32_16x16x32_bf16 v[30:33], v[180:183], v[220:223], 0
	v_mfma_f32_16x16x32_bf16 v[10:13], v[188:191], v[220:223], 0
	v_mfma_f32_16x16x32_bf16 v[6:9], v[184:187], v[200:203], v[6:9]
	v_mfma_f32_16x16x32_bf16 v[2:5], v[192:195], v[200:203], v[2:5]
	v_mfma_f32_16x16x32_bf16 v[18:21], v[184:187], v[208:211], v[18:21]
	v_mfma_f32_16x16x32_bf16 v[14:17], v[192:195], v[208:211], v[14:17]
	v_mfma_f32_16x16x32_bf16 v[26:29], v[184:187], v[216:219], v[26:29]
	v_mfma_f32_16x16x32_bf16 v[22:25], v[192:195], v[216:219], v[22:25]
	v_mfma_f32_16x16x32_bf16 v[30:33], v[184:187], v[224:227], v[30:33]
	v_mfma_f32_16x16x32_bf16 v[10:13], v[192:195], v[224:227], v[10:13]
	s_barrier
	s_add_i32 s72, 0, 0x18000
	v_add_u32_e32 v138, s72, v174
	s_add_i32 s73, 0, 0x1c000
	ds_read_b128 v[156:159], v138
	ds_read_b128 v[160:163], v138 offset:1024
	ds_read_b128 v[164:167], v138 offset:2048
	ds_read_b128 v[168:171], v138 offset:3072
	v_add_u32_e32 v138, s73, v174
	ds_read_b128 v[180:183], v138
	ds_read_b128 v[184:187], v138 offset:1024
	ds_read_b128 v[188:191], v138 offset:2048
	ds_read_b128 v[192:195], v138 offset:3072
	s_add_u32 s50, s50, 0x80000
	s_addc_u32 s51, s51, 0
	s_mov_b32 m0, s55
	v_lshl_add_u64 v[234:235], s[50:51], 0, v[130:131]
	ds_read_b128 v[196:199], v178 offset:32768
	ds_read_b128 v[200:203], v178 offset:33792
	ds_read_b128 v[204:207], v178 offset:34816
	ds_read_b128 v[208:211], v178 offset:35840
	ds_read_b128 v[212:215], v178 offset:36864
	ds_read_b128 v[216:219], v178 offset:37888
	ds_read_b128 v[220:223], v178 offset:38912
	ds_read_b128 v[224:227], v178 offset:39936
	global_load_lds_dwordx4 v[234:235], off
	v_lshl_add_u64 v[234:235], s[50:51], 0, v[134:135]
	s_mov_b32 m0, s56
	s_nop 0
	global_load_lds_dwordx4 v[234:235], off
	s_waitcnt vmcnt(8)
	s_waitcnt lgkmcnt(0)
	s_barrier
	v_mfma_f32_16x16x32_bf16 v[126:129], v[156:159], v[196:199], v[126:129]
	v_mfma_f32_16x16x32_bf16 v[122:125], v[164:167], v[196:199], v[122:125]
	v_mfma_f32_16x16x32_bf16 v[118:121], v[156:159], v[204:207], v[118:121]
	v_mfma_f32_16x16x32_bf16 v[114:117], v[164:167], v[204:207], v[114:117]
	v_mfma_f32_16x16x32_bf16 v[110:113], v[156:159], v[212:215], v[110:113]
	v_mfma_f32_16x16x32_bf16 v[106:109], v[164:167], v[212:215], v[106:109]
	v_mfma_f32_16x16x32_bf16 v[102:105], v[156:159], v[220:223], v[102:105]
	v_mfma_f32_16x16x32_bf16 v[98:101], v[164:167], v[220:223], v[98:101]
	v_mfma_f32_16x16x32_bf16 v[126:129], v[160:163], v[200:203], v[126:129]
	v_mfma_f32_16x16x32_bf16 v[122:125], v[168:171], v[200:203], v[122:125]
	v_mfma_f32_16x16x32_bf16 v[118:121], v[160:163], v[208:211], v[118:121]
	v_mfma_f32_16x16x32_bf16 v[114:117], v[168:171], v[208:211], v[114:117]
	v_mfma_f32_16x16x32_bf16 v[110:113], v[160:163], v[216:219], v[110:113]
	v_mfma_f32_16x16x32_bf16 v[106:109], v[168:171], v[216:219], v[106:109]
	v_mfma_f32_16x16x32_bf16 v[102:105], v[160:163], v[224:227], v[102:105]
	v_mfma_f32_16x16x32_bf16 v[98:101], v[168:171], v[224:227], v[98:101]
	v_mfma_f32_16x16x32_bf16 v[38:41], v[180:183], v[196:199], v[38:41]
	v_mfma_f32_16x16x32_bf16 v[34:37], v[188:191], v[196:199], v[34:37]
	v_mfma_f32_16x16x32_bf16 v[46:49], v[180:183], v[204:207], v[46:49]
	v_mfma_f32_16x16x32_bf16 v[42:45], v[188:191], v[204:207], v[42:45]
	v_mfma_f32_16x16x32_bf16 v[54:57], v[180:183], v[212:215], v[54:57]
	v_mfma_f32_16x16x32_bf16 v[50:53], v[188:191], v[212:215], v[50:53]
	v_mfma_f32_16x16x32_bf16 v[62:65], v[180:183], v[220:223], v[62:65]
	v_mfma_f32_16x16x32_bf16 v[58:61], v[188:191], v[220:223], v[58:61]
	v_mfma_f32_16x16x32_bf16 v[38:41], v[184:187], v[200:203], v[38:41]
	v_mfma_f32_16x16x32_bf16 v[34:37], v[192:195], v[200:203], v[34:37]
	v_mfma_f32_16x16x32_bf16 v[46:49], v[184:187], v[208:211], v[46:49]
	v_mfma_f32_16x16x32_bf16 v[42:45], v[192:195], v[208:211], v[42:45]
	v_mfma_f32_16x16x32_bf16 v[54:57], v[184:187], v[216:219], v[54:57]
	v_mfma_f32_16x16x32_bf16 v[50:53], v[192:195], v[216:219], v[50:53]
	v_mfma_f32_16x16x32_bf16 v[62:65], v[184:187], v[224:227], v[62:65]
	v_mfma_f32_16x16x32_bf16 v[58:61], v[192:195], v[224:227], v[58:61]
	s_barrier
	s_add_i32 s50, s72, s52
	v_lshl_add_u64 v[172:173], v[172:173], 0, s[6:7]
	s_mov_b32 m0, s50
	ds_read_b128 v[196:199], v178 offset:49152
	ds_read_b128 v[200:203], v178 offset:50176
	ds_read_b128 v[204:207], v178 offset:51200
	ds_read_b128 v[208:211], v178 offset:52224
	ds_read_b128 v[212:215], v178 offset:53248
	ds_read_b128 v[216:219], v178 offset:54272
	ds_read_b128 v[220:223], v178 offset:55296
	ds_read_b128 v[224:227], v178 offset:56320
	global_load_lds_dwordx4 v[172:173], off
	s_add_i32 m0, s50, 0x2000
	s_add_u32 s48, s48, 0x80080
	v_lshl_add_u64 v[172:173], v[228:229], 0, s[6:7]
	s_addc_u32 s49, s49, 0
	s_add_i32 s50, s73, s52
	global_load_lds_dwordx4 v[172:173], off
	v_lshl_add_u64 v[172:173], s[48:49], 0, v[132:133]
	s_mov_b32 m0, s50
	s_nop 0
	global_load_lds_dwordx4 v[172:173], off
	v_lshl_add_u64 v[172:173], s[48:49], 0, v[136:137]
	s_add_i32 m0, s50, 0x2000
	s_nop 0
	global_load_lds_dwordx4 v[172:173], off
	v_lshl_add_u64 v[172:173], v[230:231], 0, s[6:7]
	s_mov_b32 m0, s61
	s_nop 0
	global_load_lds_dwordx4 v[172:173], off
	v_lshl_add_u64 v[172:173], v[232:233], 0, s[6:7]
	s_mov_b32 m0, s62
	s_nop 0
	global_load_lds_dwordx4 v[172:173], off
	s_waitcnt vmcnt(8)
	s_waitcnt lgkmcnt(0)
	s_barrier
	v_mfma_f32_16x16x32_bf16 v[94:97], v[156:159], v[196:199], v[94:97]
	v_mfma_f32_16x16x32_bf16 v[90:93], v[164:167], v[196:199], v[90:93]
	v_mfma_f32_16x16x32_bf16 v[86:89], v[156:159], v[204:207], v[86:89]
	v_mfma_f32_16x16x32_bf16 v[82:85], v[164:167], v[204:207], v[82:85]
	v_mfma_f32_16x16x32_bf16 v[78:81], v[156:159], v[212:215], v[78:81]
	v_mfma_f32_16x16x32_bf16 v[74:77], v[164:167], v[212:215], v[74:77]
	v_mfma_f32_16x16x32_bf16 v[70:73], v[156:159], v[220:223], v[70:73]
	v_mfma_f32_16x16x32_bf16 v[66:69], v[164:167], v[220:223], v[66:69]
	v_mfma_f32_16x16x32_bf16 v[94:97], v[160:163], v[200:203], v[94:97]
	v_mfma_f32_16x16x32_bf16 v[90:93], v[168:171], v[200:203], v[90:93]
	v_mfma_f32_16x16x32_bf16 v[86:89], v[160:163], v[208:211], v[86:89]
	v_mfma_f32_16x16x32_bf16 v[82:85], v[168:171], v[208:211], v[82:85]
	v_mfma_f32_16x16x32_bf16 v[78:81], v[160:163], v[216:219], v[78:81]
	v_mfma_f32_16x16x32_bf16 v[74:77], v[168:171], v[216:219], v[74:77]
	v_mfma_f32_16x16x32_bf16 v[70:73], v[160:163], v[224:227], v[70:73]
	v_mfma_f32_16x16x32_bf16 v[66:69], v[168:171], v[224:227], v[66:69]
	v_mfma_f32_16x16x32_bf16 v[6:9], v[180:183], v[196:199], v[6:9]
	v_mfma_f32_16x16x32_bf16 v[2:5], v[188:191], v[196:199], v[2:5]
	v_mfma_f32_16x16x32_bf16 v[18:21], v[180:183], v[204:207], v[18:21]
	v_mfma_f32_16x16x32_bf16 v[14:17], v[188:191], v[204:207], v[14:17]
	v_mfma_f32_16x16x32_bf16 v[26:29], v[180:183], v[212:215], v[26:29]
	v_mfma_f32_16x16x32_bf16 v[22:25], v[188:191], v[212:215], v[22:25]
	v_mfma_f32_16x16x32_bf16 v[30:33], v[180:183], v[220:223], v[30:33]
	v_mfma_f32_16x16x32_bf16 v[10:13], v[188:191], v[220:223], v[10:13]
	v_mfma_f32_16x16x32_bf16 v[6:9], v[184:187], v[200:203], v[6:9]
	v_mfma_f32_16x16x32_bf16 v[2:5], v[192:195], v[200:203], v[2:5]
	v_mfma_f32_16x16x32_bf16 v[18:21], v[184:187], v[208:211], v[18:21]
	v_mfma_f32_16x16x32_bf16 v[14:17], v[192:195], v[208:211], v[14:17]
	v_mfma_f32_16x16x32_bf16 v[26:29], v[184:187], v[216:219], v[26:29]
	v_mfma_f32_16x16x32_bf16 v[22:25], v[192:195], v[216:219], v[22:25]
	v_mfma_f32_16x16x32_bf16 v[30:33], v[184:187], v[224:227], v[30:33]
	v_mfma_f32_16x16x32_bf16 v[10:13], v[192:195], v[224:227], v[10:13]
	s_barrier
	s_add_i32 s71, s71, 2
	s_add_u32 s46, s46, 0x100
	s_addc_u32 s47, s47, 0
	s_add_u32 s69, s69, 0x100
	s_addc_u32 s70, s70, 0
	s_cmp_gt_u32 s71, 29

.LBB0_2107:
	s_setprio 0
	v_readlane_b32 s26, v254, 1
	v_readlane_b32 s27, v254, 2
	s_mov_b32 s23, s99
	s_add_i32 s46, s46, 1
	s_mul_i32 s4, s46, s49
	s_waitcnt lgkmcnt(0)
	ds_read_b128 v[154:157], v150
	ds_read_b128 v[158:161], v150 offset:1024
	ds_read_b128 v[162:165], v150 offset:2048
	ds_read_b128 v[166:169], v150 offset:3072
	ds_read_b128 v[170:173], v151
	ds_read_b128 v[174:177], v151 offset:1024
	ds_read_b128 v[178:181], v151 offset:2048
	ds_read_b128 v[182:185], v151 offset:3072
	ds_read_b128 v[186:189], v152
	ds_read_b128 v[190:193], v152 offset:1024
	ds_read_b128 v[194:197], v152 offset:2048
	ds_read_b128 v[198:201], v152 offset:3072
	ds_read_b128 v[202:205], v152 offset:4096
	ds_read_b128 v[206:209], v152 offset:5120
	ds_read_b128 v[210:213], v152 offset:6144
	ds_read_b128 v[214:217], v152 offset:7168
	s_mul_hi_u32 s5, s46, s23
	s_add_i32 s5, s5, s4
	s_mul_i32 s4, s46, s23
	v_readlane_b32 s23, v254, 14
	s_add_u32 s26, s4, s23
	s_addc_u32 s27, s5, s33
	v_cmp_gt_i64_e32 vcc, s[26:27], v[144:145]
	v_cmp_lt_i64_e64 s[4:5], s[26:27], v[142:143]
	s_cbranch_vccnz .LBB0_2113
	s_ashr_i32 s22, s26, 31
	s_lshr_b32 s22, s22, 29
	s_add_i32 s24, s26, s22
	s_and_b32 s22, s24, -8
	s_sub_i32 s25, s26, s22
	s_cmp_gt_i32 s25, -1
	s_mov_b64 s[22:23], -1
	s_cbranch_scc0 .LBB0_2110
	s_lshl_b32 s26, s25, 7
	s_mov_b64 s[22:23], 0

.LBB0_2363:
	s_setprio 0
	v_readlane_b32 s26, v254, 1
	v_readlane_b32 s27, v254, 2
	s_mov_b32 s23, s99
	s_add_i32 s7, s7, 1
	s_mul_i32 s4, s7, s59
	s_waitcnt lgkmcnt(0)
	ds_read_b128 v[18:21], v186
	ds_read_b128 v[22:25], v186 offset:1024
	ds_read_b128 v[26:29], v186 offset:2048
	ds_read_b128 v[30:33], v186 offset:3072
	ds_read_b128 v[2:5], v187
	ds_read_b128 v[6:9], v187 offset:1024
	ds_read_b128 v[10:13], v187 offset:2048
	ds_read_b128 v[14:17], v187 offset:3072
	ds_read_b128 v[176:179], v188
	ds_read_b128 v[180:183], v188 offset:1024
	ds_read_b128 v[192:195], v188 offset:2048
	ds_read_b128 v[196:199], v188 offset:3072
	ds_read_b128 v[200:203], v188 offset:4096
	ds_read_b128 v[204:207], v188 offset:5120
	ds_read_b128 v[216:219], v188 offset:6144
	ds_read_b128 v[220:223], v188 offset:7168
	s_mul_hi_u32 s5, s7, s23
	s_add_i32 s5, s5, s4
	s_mul_i32 s4, s7, s23
	v_readlane_b32 s23, v254, 14
	s_add_u32 s26, s4, s23
	s_addc_u32 s27, s5, s45
	v_cmp_ge_i64_e32 vcc, s[26:27], v[174:175]
	v_cmp_lt_i64_e64 s[4:5], s[26:27], v[174:175]
	s_cbranch_vccnz .LBB0_2365
	s_ashr_i32 s22, s26, 31
	s_lshr_b32 s22, s22, 29
	s_add_i32 s22, s26, s22
	s_ashr_i32 s23, s22, 3
	s_and_b32 s22, s22, -8
	s_sub_i32 s22, s26, s22
	s_cmp_lt_i32 s22, 0
	s_cselect_b32 s24, s46, s44
	s_mul_i32 s22, s24, s22
	s_add_i32 s22, s22, s23
	s_mul_hi_i32 s23, s22, 0x92492493
	s_add_i32 s23, s23, s22
	s_lshr_b32 s24, s23, 31
	s_ashr_i32 s23, s23, 8
	s_add_i32 s23, s23, s24
	s_lshl_b32 s24, s23, 3
	s_sub_i32 s25, s58, s24
	s_min_i32 s25, s25, 8
	s_abs_i32 s26, s25
	v_cvt_f32_u32_e32 v210, s26
	s_sub_i32 s28, 0, s26
	s_mulk_i32 s23, 0x1c0
	s_sub_i32 s22, s22, s23
	v_rcp_iflag_f32_e32 v210, v210
	s_abs_i32 s23, s22
	s_xor_b32 s27, s22, s25
	s_ashr_i32 s27, s27, 31
	v_mul_f32_e32 v210, 0x4f7ffffe, v210
	v_cvt_u32_f32_e32 v210, v210
	s_nop 0
	v_readfirstlane_b32 s29, v210
	s_mul_i32 s28, s28, s29
	s_mul_hi_u32 s28, s29, s28
	s_add_i32 s29, s29, s28
	s_mul_hi_u32 s28, s23, s29
	s_mul_i32 s29, s28, s26
	s_sub_i32 s23, s23, s29
	s_add_i32 s38, s28, 1
	s_sub_i32 s29, s23, s26
	s_cmp_ge_u32 s23, s26
	s_cselect_b32 s28, s38, s28
	s_cselect_b32 s23, s29, s23
	s_add_i32 s29, s28, 1
	s_cmp_ge_u32 s23, s26
	s_cselect_b32 s23, s29, s28
	s_xor_b32 s23, s23, s27
	s_sub_i32 s64, s23, s27
	s_mul_i32 s23, s64, s25
	s_sub_i32 s22, s22, s23
	s_add_i32 s22, s22, s24
	s_cmp_ge_i32 s22, s57
	s_cselect_b64 s[24:25], -1, 0
	s_cmp_ge_i32 s22, s33
	v_cndmask_b32_e64 v210, 0, 1, s[24:25]
	s_cselect_b64 s[24:25], -1, 0
	s_cmp_ge_i32 s22, s52
	v_cndmask_b32_e64 v211, 0, 1, s[24:25]
	s_cselect_b64 s[24:25], -1, 0
	v_readfirstlane_b32 s23, v211
	v_readfirstlane_b32 s26, v210
	s_cmp_lg_u64 s[24:25], 0
	s_addc_u32 s23, s23, s26
	s_cmp_ge_i32 s22, s53
	s_cselect_b64 s[24:25], -1, 0
	s_cmp_ge_i32 s22, s54
	v_cndmask_b32_e64 v210, 0, 1, s[24:25]
	s_cselect_b64 s[24:25], -1, 0
	v_readfirstlane_b32 s26, v210
	s_cmp_lg_u64 s[24:25], 0
	s_addc_u32 s23, s23, s26
	s_cmp_ge_i32 s22, s55
	s_cselect_b64 s[24:25], -1, 0
	s_cmp_ge_i32 s22, s56
	v_cndmask_b32_e64 v210, 0, 1, s[24:25]
	s_cselect_b64 s[24:25], -1, 0
	v_readfirstlane_b32 s26, v210
	s_cmp_lg_u64 s[24:25], 0
	s_addc_u32 s23, s23, s26
	s_mul_i32 s23, s23, 56
	s_add_i32 s24, s23, s64
